# part D conversion in FFN1 epilogue: loads issued at epilogue start into dead LDS-fragment registers, nt hint on the streaming loads/stores
# baseline (speedup 1.0000x reference)
.LBB0_1912:
	s_lshl_b32 s72, s32, 8
	s_add_i32 s72, s72, s2
	s_cmpk_ge_i32 s72, 7136
	s_cbranch_scc1 .Lcvd_p1_end
	v_readlane_b32 s78, v255, 40
	v_readlane_b32 s79, v255, 41
	s_addk_i32 s72, 1056
	s_lshr_b32 s80, s72, 4
	s_lshl_b32 s80, s80, 18
	s_and_b32 s81, s72, 15
	s_lshl_b32 s81, s81, 8
	s_add_i32 s80, s80, s81
	v_and_b32_e32 v230, 63, v0
	v_lshl_add_u32 v230, v230, 2, s80
	v_add_u32_e32 v211, 0x1000, v230
	v_add_u32_e32 v212, 0x2000, v230
	v_add_u32_e32 v213, 0x3000, v230
	v_add_u32_e32 v214, 0x4000, v230
	v_add_u32_e32 v215, 0x5000, v230
	v_add_u32_e32 v216, 0x6000, v230
	v_add_u32_e32 v217, 0x7000, v230
	global_load_dword v210, v230, s[78:79] nt
	global_load_dword v211, v211, s[78:79] nt
	global_load_dword v212, v212, s[78:79] nt
	global_load_dword v213, v213, s[78:79] nt
	global_load_dword v214, v214, s[78:79] nt
	global_load_dword v215, v215, s[78:79] nt
	global_load_dword v216, v216, s[78:79] nt
	global_load_dword v217, v217, s[78:79] nt
	s_cmpk_ge_i32 s72, 7936
	s_cbranch_scc1 .Lcvd_p1_end
	v_add_u32_e32 v218, 0x400000, v230
	v_add_u32_e32 v219, 0x401000, v230
	v_add_u32_e32 v220, 0x402000, v230
	v_add_u32_e32 v221, 0x403000, v230
	v_add_u32_e32 v222, 0x404000, v230
	v_add_u32_e32 v223, 0x405000, v230
	v_add_u32_e32 v224, 0x406000, v230
	v_add_u32_e32 v225, 0x407000, v230
	global_load_dword v218, v218, s[78:79] nt
	global_load_dword v219, v219, s[78:79] nt
	global_load_dword v220, v220, s[78:79] nt
	global_load_dword v221, v221, s[78:79] nt
	global_load_dword v222, v222, s[78:79] nt
	global_load_dword v223, v223, s[78:79] nt
	global_load_dword v224, v224, s[78:79] nt
	global_load_dword v225, v225, s[78:79] nt
.Lcvd_p1_end:
	v_mul_f32_e32 v2, 0xbfb8aa3b, v162
	v_mul_f32_e32 v6, 0xbfb8aa3b, v163
	v_exp_f32_e32 v2, v2
	v_exp_f32_e32 v6, v6
	v_mul_f32_e32 v7, 0xbfb8aa3b, v164
	v_mul_f32_e32 v8, 0xbfb8aa3b, v165
	v_add_f32_e32 v2, 1.0, v2
	v_add_f32_e32 v6, 1.0, v6
	v_exp_f32_e32 v7, v7
	v_exp_f32_e32 v8, v8
	v_mul_f32_e32 v9, 0xbfb8aa3b, v154
	v_mul_f32_e32 v10, 0xbfb8aa3b, v155
	v_rcp_f32_e32 v2, v2
	v_rcp_f32_e32 v6, v6
	v_exp_f32_e32 v9, v9
	v_exp_f32_e32 v10, v10
	v_add_f32_e32 v7, 1.0, v7
	v_add_f32_e32 v8, 1.0, v8
	v_mul_f32_e32 v11, 0xbfb8aa3b, v156
	v_mul_f32_e32 v12, 0xbfb8aa3b, v157
	v_mul_f32_e32 v2, v162, v2
	v_mul_f32_e32 v6, v163, v6
	v_rcp_f32_e32 v7, v7
	v_rcp_f32_e32 v8, v8
	v_add_f32_e32 v9, 1.0, v9
	v_add_f32_e32 v10, 1.0, v10
	v_exp_f32_e32 v11, v11
	v_exp_f32_e32 v12, v12
	v_mul_f32_e32 v2, v2, v158
	v_mul_f32_e32 v6, v6, v159
	v_rcp_f32_e32 v9, v9
	v_rcp_f32_e32 v10, v10
	v_med3_f32 v2, v2, s7, v228
	v_med3_f32 v13, v6, s7, v228
	v_mov_b32_e32 v6, v3
	v_cvt_pk_fp8_f32 v6, v2, v13
	v_mul_f32_e32 v7, v164, v7
	v_mul_f32_e32 v8, v165, v8
	v_add_f32_e32 v11, 1.0, v11
	v_add_f32_e32 v12, 1.0, v12
	v_mul_f32_e32 v7, v7, v160
	v_mul_f32_e32 v8, v8, v161
	v_mul_f32_e32 v9, v154, v9
	v_mul_f32_e32 v10, v155, v10
	v_rcp_f32_e32 v11, v11
	v_rcp_f32_e32 v12, v12
	v_mul_f32_e32 v9, v9, v150
	v_mul_f32_e32 v10, v10, v151
	v_med3_f32 v2, v7, s7, v228
	v_med3_f32 v7, v8, s7, v228
	v_cvt_pk_fp8_f32 v6, v2, v7 op_sel:[0,0,1]
	v_med3_f32 v2, v9, s7, v228
	v_med3_f32 v8, v10, s7, v228
	v_mov_b32_e32 v7, v3
	v_cvt_pk_fp8_f32 v7, v2, v8
	v_lshl_add_u32 v4, s48, 8, v181
	v_mul_f32_e32 v11, v156, v11
	v_mul_f32_e32 v12, v157, v12
	v_ashrrev_i32_e32 v5, 31, v4
	v_mul_f32_e32 v11, v11, v152
	v_mul_f32_e32 v12, v12, v153
	v_lshlrev_b64 v[4:5], 11, v[4:5]
	s_lshl_b32 s0, s3, 7
	v_med3_f32 v2, v11, s7, v228
	v_med3_f32 v8, v12, s7, v228
	v_lshl_add_u64 v[4:5], s[40:41], 0, v[4:5]
	s_ashr_i32 s1, s0, 31
	v_cvt_pk_fp8_f32 v7, v2, v8 op_sel:[0,0,1]
	v_lshl_add_u64 v[4:5], v[4:5], 0, s[0:1]
	v_lshl_add_u64 v[4:5], v[4:5], 0, s[76:77]
	v_lshl_add_u64 v[4:5], v[4:5], 0, v[170:171]
	s_nop 15
	s_nop 15
	global_store_dwordx2 v[4:5], v[6:7], off
	v_mul_f32_e32 v2, 0xbfb8aa3b, v146
	v_mul_f32_e32 v6, 0xbfb8aa3b, v147
	v_exp_f32_e32 v2, v2
	v_exp_f32_e32 v6, v6
	v_mul_f32_e32 v7, 0xbfb8aa3b, v148
	v_mul_f32_e32 v8, 0xbfb8aa3b, v149
	v_add_f32_e32 v2, 1.0, v2
	v_add_f32_e32 v6, 1.0, v6
	v_exp_f32_e32 v7, v7
	v_exp_f32_e32 v8, v8
	v_mul_f32_e32 v9, 0xbfb8aa3b, v138
	v_mul_f32_e32 v10, 0xbfb8aa3b, v139
	v_rcp_f32_e32 v2, v2
	v_rcp_f32_e32 v6, v6
	v_exp_f32_e32 v9, v9
	v_exp_f32_e32 v10, v10
	v_add_f32_e32 v7, 1.0, v7
	v_add_f32_e32 v8, 1.0, v8
	v_mul_f32_e32 v11, 0xbfb8aa3b, v140
	v_mul_f32_e32 v12, 0xbfb8aa3b, v141
	v_mul_f32_e32 v2, v146, v2
	v_mul_f32_e32 v6, v147, v6
	v_rcp_f32_e32 v7, v7
	v_rcp_f32_e32 v8, v8
	v_add_f32_e32 v9, 1.0, v9
	v_add_f32_e32 v10, 1.0, v10
	v_exp_f32_e32 v11, v11
	v_exp_f32_e32 v12, v12
	v_mul_f32_e32 v2, v2, v142
	v_mul_f32_e32 v6, v6, v143
	v_rcp_f32_e32 v9, v9
	v_rcp_f32_e32 v10, v10
	v_med3_f32 v2, v2, s7, v228
	v_med3_f32 v13, v6, s7, v228
	v_mov_b32_e32 v6, v3
	v_cvt_pk_fp8_f32 v6, v2, v13
	v_mul_f32_e32 v7, v148, v7
	v_mul_f32_e32 v8, v149, v8
	v_add_f32_e32 v11, 1.0, v11
	v_add_f32_e32 v12, 1.0, v12
	v_mul_f32_e32 v7, v7, v144
	v_mul_f32_e32 v8, v8, v145
	v_mul_f32_e32 v9, v138, v9
	v_mul_f32_e32 v10, v139, v10
	v_rcp_f32_e32 v11, v11
	v_rcp_f32_e32 v12, v12
	v_mul_f32_e32 v9, v9, v134
	v_mul_f32_e32 v10, v10, v135
	v_med3_f32 v2, v7, s7, v228
	v_med3_f32 v7, v8, s7, v228
	v_cvt_pk_fp8_f32 v6, v2, v7 op_sel:[0,0,1]
	v_med3_f32 v2, v9, s7, v228
	v_med3_f32 v8, v10, s7, v228
	v_mov_b32_e32 v7, v3
	v_cvt_pk_fp8_f32 v7, v2, v8
	v_mul_f32_e32 v11, v140, v11
	v_mul_f32_e32 v12, v141, v12
	v_mul_f32_e32 v11, v11, v136
	v_mul_f32_e32 v12, v12, v137
	v_med3_f32 v2, v11, s7, v228
	v_med3_f32 v8, v12, s7, v228
	v_cvt_pk_fp8_f32 v7, v2, v8 op_sel:[0,0,1]
	v_add_co_u32_e32 v8, vcc, s31, v4
	v_mul_f32_e32 v2, 0xbfb8aa3b, v130
	s_nop 0
	v_addc_co_u32_e32 v9, vcc, 0, v5, vcc
	global_store_dwordx2 v[8:9], v[6:7], off
	v_mul_f32_e32 v6, 0xbfb8aa3b, v131
	v_exp_f32_e32 v2, v2
	v_exp_f32_e32 v6, v6
	v_mul_f32_e32 v7, 0xbfb8aa3b, v132
	v_mul_f32_e32 v8, 0xbfb8aa3b, v133
	v_add_f32_e32 v2, 1.0, v2
	v_add_f32_e32 v6, 1.0, v6
	v_exp_f32_e32 v7, v7
	v_exp_f32_e32 v8, v8
	v_mul_f32_e32 v9, 0xbfb8aa3b, v122
	v_mul_f32_e32 v10, 0xbfb8aa3b, v123
	v_rcp_f32_e32 v2, v2
	v_rcp_f32_e32 v6, v6
	v_exp_f32_e32 v9, v9
	v_exp_f32_e32 v10, v10
	v_add_f32_e32 v7, 1.0, v7
	v_add_f32_e32 v8, 1.0, v8
	v_mul_f32_e32 v11, 0xbfb8aa3b, v124
	v_mul_f32_e32 v12, 0xbfb8aa3b, v125
	v_mul_f32_e32 v2, v130, v2
	v_mul_f32_e32 v6, v131, v6
	v_rcp_f32_e32 v7, v7
	v_rcp_f32_e32 v8, v8
	v_add_f32_e32 v9, 1.0, v9
	v_add_f32_e32 v10, 1.0, v10
	v_exp_f32_e32 v11, v11
	v_exp_f32_e32 v12, v12
	v_mul_f32_e32 v2, v2, v126
	v_mul_f32_e32 v6, v6, v127
	v_rcp_f32_e32 v9, v9
	v_rcp_f32_e32 v10, v10
	v_med3_f32 v2, v2, s7, v228
	v_med3_f32 v13, v6, s7, v228
	v_mov_b32_e32 v6, v3
	v_cvt_pk_fp8_f32 v6, v2, v13
	v_mul_f32_e32 v7, v132, v7
	v_mul_f32_e32 v8, v133, v8
	v_add_f32_e32 v11, 1.0, v11
	v_add_f32_e32 v12, 1.0, v12
	v_mul_f32_e32 v7, v7, v128
	v_mul_f32_e32 v8, v8, v129
	v_mul_f32_e32 v9, v122, v9
	v_mul_f32_e32 v10, v123, v10
	v_rcp_f32_e32 v11, v11
	v_rcp_f32_e32 v12, v12
	v_mul_f32_e32 v9, v9, v118
	v_mul_f32_e32 v10, v10, v119
	v_med3_f32 v2, v7, s7, v228
	v_med3_f32 v7, v8, s7, v228
	v_cvt_pk_fp8_f32 v6, v2, v7 op_sel:[0,0,1]
	v_med3_f32 v2, v9, s7, v228
	v_med3_f32 v8, v10, s7, v228
	v_mov_b32_e32 v7, v3
	v_cvt_pk_fp8_f32 v7, v2, v8
	v_mul_f32_e32 v11, v124, v11
	v_mul_f32_e32 v12, v125, v12
	v_mul_f32_e32 v11, v11, v120
	v_mul_f32_e32 v12, v12, v121
	v_med3_f32 v2, v11, s7, v228
	v_med3_f32 v8, v12, s7, v228
	v_cvt_pk_fp8_f32 v7, v2, v8 op_sel:[0,0,1]
	s_mov_b32 s0, 0x10000
	v_add_co_u32_e32 v8, vcc, s0, v4
	v_mul_f32_e32 v2, 0xbfb8aa3b, v112
	s_nop 0
	v_addc_co_u32_e32 v9, vcc, 0, v5, vcc
	global_store_dwordx2 v[8:9], v[6:7], off
	v_mul_f32_e32 v6, 0xbfb8aa3b, v113
	v_exp_f32_e32 v2, v2
	v_exp_f32_e32 v6, v6
	v_mul_f32_e32 v7, 0xbfb8aa3b, v114
	v_mul_f32_e32 v8, 0xbfb8aa3b, v115
	v_add_f32_e32 v2, 1.0, v2
	v_add_f32_e32 v6, 1.0, v6
	v_exp_f32_e32 v7, v7
	v_exp_f32_e32 v8, v8
	v_mul_f32_e32 v9, 0xbfb8aa3b, v104
	v_mul_f32_e32 v10, 0xbfb8aa3b, v105
	v_rcp_f32_e32 v2, v2
	v_rcp_f32_e32 v6, v6
	v_exp_f32_e32 v9, v9
	v_exp_f32_e32 v10, v10
	v_add_f32_e32 v7, 1.0, v7
	v_add_f32_e32 v8, 1.0, v8
	v_mul_f32_e32 v11, 0xbfb8aa3b, v106
	v_mul_f32_e32 v12, 0xbfb8aa3b, v107
	v_mul_f32_e32 v2, v112, v2
	v_mul_f32_e32 v6, v113, v6
	v_rcp_f32_e32 v7, v7
	v_rcp_f32_e32 v8, v8
	v_add_f32_e32 v9, 1.0, v9
	v_add_f32_e32 v10, 1.0, v10
	v_exp_f32_e32 v11, v11
	v_exp_f32_e32 v12, v12
	v_mul_f32_e32 v2, v2, v108
	v_mul_f32_e32 v6, v6, v109
	v_rcp_f32_e32 v9, v9
	v_rcp_f32_e32 v10, v10
	v_med3_f32 v2, v2, s7, v228
	v_med3_f32 v13, v6, s7, v228
	v_mov_b32_e32 v6, v3
	v_cvt_pk_fp8_f32 v6, v2, v13
	v_mul_f32_e32 v7, v114, v7
	v_mul_f32_e32 v8, v115, v8
	v_add_f32_e32 v11, 1.0, v11
	v_add_f32_e32 v12, 1.0, v12
	v_mul_f32_e32 v7, v7, v110
	v_mul_f32_e32 v8, v8, v111
	v_mul_f32_e32 v9, v104, v9
	v_mul_f32_e32 v10, v105, v10
	v_rcp_f32_e32 v11, v11
	v_rcp_f32_e32 v12, v12
	v_mul_f32_e32 v9, v9, v100
	v_mul_f32_e32 v10, v10, v101
	v_med3_f32 v2, v7, s7, v228
	v_med3_f32 v7, v8, s7, v228
	v_cvt_pk_fp8_f32 v6, v2, v7 op_sel:[0,0,1]
	v_med3_f32 v2, v9, s7, v228
	v_med3_f32 v8, v10, s7, v228
	v_mov_b32_e32 v7, v3
	v_cvt_pk_fp8_f32 v7, v2, v8
	v_mul_f32_e32 v11, v106, v11
	v_mul_f32_e32 v12, v107, v12
	v_mul_f32_e32 v11, v11, v102
	v_mul_f32_e32 v12, v12, v103
	v_med3_f32 v2, v11, s7, v228
	v_med3_f32 v8, v12, s7, v228
	v_cvt_pk_fp8_f32 v7, v2, v8 op_sel:[0,0,1]
	s_mov_b32 s0, 0x18000
	v_add_co_u32_e32 v8, vcc, s0, v4
	v_mul_f32_e32 v2, 0xbfb8aa3b, v96
	s_nop 0
	v_addc_co_u32_e32 v9, vcc, 0, v5, vcc
	global_store_dwordx2 v[8:9], v[6:7], off
	v_mul_f32_e32 v6, 0xbfb8aa3b, v97
	v_exp_f32_e32 v2, v2
	v_exp_f32_e32 v6, v6
	v_mul_f32_e32 v7, 0xbfb8aa3b, v98
	v_mul_f32_e32 v8, 0xbfb8aa3b, v99
	v_add_f32_e32 v2, 1.0, v2
	v_add_f32_e32 v6, 1.0, v6
	v_exp_f32_e32 v7, v7
	v_exp_f32_e32 v8, v8
	v_mul_f32_e32 v9, 0xbfb8aa3b, v88
	v_mul_f32_e32 v10, 0xbfb8aa3b, v89
	v_rcp_f32_e32 v2, v2
	v_rcp_f32_e32 v6, v6
	v_exp_f32_e32 v9, v9
	v_exp_f32_e32 v10, v10
	v_add_f32_e32 v7, 1.0, v7
	v_add_f32_e32 v8, 1.0, v8
	v_mul_f32_e32 v11, 0xbfb8aa3b, v90
	v_mul_f32_e32 v12, 0xbfb8aa3b, v91
	v_mul_f32_e32 v2, v96, v2
	v_mul_f32_e32 v6, v97, v6
	v_rcp_f32_e32 v7, v7
	v_rcp_f32_e32 v8, v8
	v_add_f32_e32 v9, 1.0, v9
	v_add_f32_e32 v10, 1.0, v10
	v_exp_f32_e32 v11, v11
	v_exp_f32_e32 v12, v12
	v_mul_f32_e32 v2, v2, v92
	v_mul_f32_e32 v6, v6, v93
	v_rcp_f32_e32 v9, v9
	v_rcp_f32_e32 v10, v10
	v_med3_f32 v2, v2, s7, v228
	v_med3_f32 v13, v6, s7, v228
	v_mov_b32_e32 v6, v3
	v_cvt_pk_fp8_f32 v6, v2, v13
	v_mul_f32_e32 v7, v98, v7
	v_mul_f32_e32 v8, v99, v8
	v_add_f32_e32 v11, 1.0, v11
	v_add_f32_e32 v12, 1.0, v12
	v_mul_f32_e32 v7, v7, v94
	v_mul_f32_e32 v8, v8, v95
	v_mul_f32_e32 v9, v88, v9
	v_mul_f32_e32 v10, v89, v10
	v_rcp_f32_e32 v11, v11
	v_rcp_f32_e32 v12, v12
	v_mul_f32_e32 v9, v9, v84
	v_mul_f32_e32 v10, v10, v85
	v_med3_f32 v2, v7, s7, v228
	v_med3_f32 v7, v8, s7, v228
	v_cvt_pk_fp8_f32 v6, v2, v7 op_sel:[0,0,1]
	v_med3_f32 v2, v9, s7, v228
	v_med3_f32 v8, v10, s7, v228
	v_mov_b32_e32 v7, v3
	v_cvt_pk_fp8_f32 v7, v2, v8
	v_mul_f32_e32 v11, v90, v11
	v_mul_f32_e32 v12, v91, v12
	v_mul_f32_e32 v11, v11, v86
	v_mul_f32_e32 v12, v12, v87
	v_med3_f32 v2, v11, s7, v228
	v_med3_f32 v8, v12, s7, v228
	v_cvt_pk_fp8_f32 v7, v2, v8 op_sel:[0,0,1]
	v_add_co_u32_e32 v8, vcc, s16, v4
	v_mul_f32_e32 v2, 0xbfb8aa3b, v80
	s_nop 0
	v_addc_co_u32_e32 v9, vcc, 0, v5, vcc
	global_store_dwordx2 v[8:9], v[6:7], off
	v_mul_f32_e32 v6, 0xbfb8aa3b, v81
	v_exp_f32_e32 v2, v2
	v_exp_f32_e32 v6, v6
	v_mul_f32_e32 v7, 0xbfb8aa3b, v82
	v_mul_f32_e32 v8, 0xbfb8aa3b, v83
	v_add_f32_e32 v2, 1.0, v2
	v_add_f32_e32 v6, 1.0, v6
	v_exp_f32_e32 v7, v7
	v_exp_f32_e32 v8, v8
	v_mul_f32_e32 v9, 0xbfb8aa3b, v72
	v_mul_f32_e32 v10, 0xbfb8aa3b, v73
	v_rcp_f32_e32 v2, v2
	v_rcp_f32_e32 v6, v6
	v_exp_f32_e32 v9, v9
	v_exp_f32_e32 v10, v10
	v_add_f32_e32 v7, 1.0, v7
	v_add_f32_e32 v8, 1.0, v8
	v_mul_f32_e32 v11, 0xbfb8aa3b, v74
	v_mul_f32_e32 v12, 0xbfb8aa3b, v75
	v_mul_f32_e32 v2, v80, v2
	v_mul_f32_e32 v6, v81, v6
	v_rcp_f32_e32 v7, v7
	v_rcp_f32_e32 v8, v8
	v_add_f32_e32 v9, 1.0, v9
	v_add_f32_e32 v10, 1.0, v10
	v_exp_f32_e32 v11, v11
	v_exp_f32_e32 v12, v12
	v_mul_f32_e32 v2, v2, v76
	v_mul_f32_e32 v6, v6, v77
	v_rcp_f32_e32 v9, v9
	v_rcp_f32_e32 v10, v10
	v_med3_f32 v2, v2, s7, v228
	v_med3_f32 v13, v6, s7, v228
	v_mov_b32_e32 v6, v3
	v_cvt_pk_fp8_f32 v6, v2, v13
	v_mul_f32_e32 v7, v82, v7
	v_mul_f32_e32 v8, v83, v8
	v_add_f32_e32 v11, 1.0, v11
	v_add_f32_e32 v12, 1.0, v12
	v_mul_f32_e32 v7, v7, v78
	v_mul_f32_e32 v8, v8, v79
	v_mul_f32_e32 v9, v72, v9
	v_mul_f32_e32 v10, v73, v10
	v_rcp_f32_e32 v11, v11
	v_rcp_f32_e32 v12, v12
	v_mul_f32_e32 v9, v9, v68
	v_mul_f32_e32 v10, v10, v69
	v_med3_f32 v2, v7, s7, v228
	v_med3_f32 v7, v8, s7, v228
	v_cvt_pk_fp8_f32 v6, v2, v7 op_sel:[0,0,1]
	v_med3_f32 v2, v9, s7, v228
	v_med3_f32 v8, v10, s7, v228
	v_mov_b32_e32 v7, v3
	v_cvt_pk_fp8_f32 v7, v2, v8
	v_mul_f32_e32 v11, v74, v11
	v_mul_f32_e32 v12, v75, v12
	v_mul_f32_e32 v11, v11, v70
	v_mul_f32_e32 v12, v12, v71
	v_med3_f32 v2, v11, s7, v228
	v_med3_f32 v8, v12, s7, v228
	v_cvt_pk_fp8_f32 v7, v2, v8 op_sel:[0,0,1]
	s_mov_b32 s0, 0x48000
	v_add_co_u32_e32 v8, vcc, s0, v4
	v_mul_f32_e32 v2, 0xbfb8aa3b, v60
	s_nop 0
	v_addc_co_u32_e32 v9, vcc, 0, v5, vcc
	global_store_dwordx2 v[8:9], v[6:7], off
	v_mul_f32_e32 v6, 0xbfb8aa3b, v61
	v_exp_f32_e32 v2, v2
	v_exp_f32_e32 v6, v6
	v_mul_f32_e32 v7, 0xbfb8aa3b, v62
	v_mul_f32_e32 v8, 0xbfb8aa3b, v63
	v_add_f32_e32 v2, 1.0, v2
	v_add_f32_e32 v6, 1.0, v6
	v_exp_f32_e32 v7, v7
	v_exp_f32_e32 v8, v8
	v_mul_f32_e32 v9, 0xbfb8aa3b, v52
	v_mul_f32_e32 v10, 0xbfb8aa3b, v53
	v_rcp_f32_e32 v2, v2
	v_rcp_f32_e32 v6, v6
	v_exp_f32_e32 v9, v9
	v_exp_f32_e32 v10, v10
	v_add_f32_e32 v7, 1.0, v7
	v_add_f32_e32 v8, 1.0, v8
	v_mul_f32_e32 v11, 0xbfb8aa3b, v54
	v_mul_f32_e32 v12, 0xbfb8aa3b, v55
	v_mul_f32_e32 v2, v60, v2
	v_mul_f32_e32 v6, v61, v6
	v_rcp_f32_e32 v7, v7
	v_rcp_f32_e32 v8, v8
	v_add_f32_e32 v9, 1.0, v9
	v_add_f32_e32 v10, 1.0, v10
	v_exp_f32_e32 v11, v11
	v_exp_f32_e32 v12, v12
	v_mul_f32_e32 v2, v2, v64
	v_mul_f32_e32 v6, v6, v65
	v_rcp_f32_e32 v9, v9
	v_rcp_f32_e32 v10, v10
	v_med3_f32 v2, v2, s7, v228
	v_med3_f32 v13, v6, s7, v228
	v_mov_b32_e32 v6, v3
	v_cvt_pk_fp8_f32 v6, v2, v13
	v_mul_f32_e32 v7, v62, v7
	v_mul_f32_e32 v8, v63, v8
	v_add_f32_e32 v11, 1.0, v11
	v_add_f32_e32 v12, 1.0, v12
	v_mul_f32_e32 v7, v7, v66
	v_mul_f32_e32 v8, v8, v67
	v_mul_f32_e32 v9, v52, v9
	v_mul_f32_e32 v10, v53, v10
	v_rcp_f32_e32 v11, v11
	v_rcp_f32_e32 v12, v12
	v_mul_f32_e32 v9, v9, v56
	v_mul_f32_e32 v10, v10, v57
	v_med3_f32 v2, v7, s7, v228
	v_med3_f32 v7, v8, s7, v228
	v_cvt_pk_fp8_f32 v6, v2, v7 op_sel:[0,0,1]
	v_med3_f32 v2, v9, s7, v228
	v_med3_f32 v8, v10, s7, v228
	v_mov_b32_e32 v7, v3
	v_cvt_pk_fp8_f32 v7, v2, v8
	v_mul_f32_e32 v11, v54, v11
	v_mul_f32_e32 v12, v55, v12
	v_mul_f32_e32 v11, v11, v58
	v_mul_f32_e32 v12, v12, v59
	v_med3_f32 v2, v11, s7, v228
	v_med3_f32 v8, v12, s7, v228
	v_cvt_pk_fp8_f32 v7, v2, v8 op_sel:[0,0,1]
	s_mov_b32 s0, 0x50000
	v_add_co_u32_e32 v8, vcc, s0, v4
	v_mul_f32_e32 v2, 0xbfb8aa3b, v44
	s_nop 0
	v_addc_co_u32_e32 v9, vcc, 0, v5, vcc
	global_store_dwordx2 v[8:9], v[6:7], off
	v_mul_f32_e32 v6, 0xbfb8aa3b, v45
	v_exp_f32_e32 v2, v2
	v_exp_f32_e32 v6, v6
	v_mul_f32_e32 v7, 0xbfb8aa3b, v46
	v_mul_f32_e32 v8, 0xbfb8aa3b, v47
	v_add_f32_e32 v2, 1.0, v2
	v_add_f32_e32 v6, 1.0, v6
	v_exp_f32_e32 v7, v7
	v_exp_f32_e32 v8, v8
	v_mul_f32_e32 v9, 0xbfb8aa3b, v36
	v_mul_f32_e32 v10, 0xbfb8aa3b, v37
	v_rcp_f32_e32 v2, v2
	v_rcp_f32_e32 v6, v6
	v_exp_f32_e32 v9, v9
	v_exp_f32_e32 v10, v10
	v_add_f32_e32 v7, 1.0, v7
	v_add_f32_e32 v8, 1.0, v8
	v_mul_f32_e32 v11, 0xbfb8aa3b, v38
	v_mul_f32_e32 v12, 0xbfb8aa3b, v39
	v_mul_f32_e32 v2, v44, v2
	v_mul_f32_e32 v6, v45, v6
	v_rcp_f32_e32 v7, v7
	v_rcp_f32_e32 v8, v8
	v_add_f32_e32 v9, 1.0, v9
	v_add_f32_e32 v10, 1.0, v10
	v_exp_f32_e32 v11, v11
	v_exp_f32_e32 v12, v12
	v_mul_f32_e32 v2, v2, v48
	v_mul_f32_e32 v6, v6, v49
	v_rcp_f32_e32 v9, v9
	v_rcp_f32_e32 v10, v10
	v_med3_f32 v2, v2, s7, v228
	v_med3_f32 v13, v6, s7, v228
	v_mov_b32_e32 v6, v3
	v_cvt_pk_fp8_f32 v6, v2, v13
	v_mul_f32_e32 v7, v46, v7
	v_mul_f32_e32 v8, v47, v8
	v_add_f32_e32 v11, 1.0, v11
	v_add_f32_e32 v12, 1.0, v12
	v_mul_f32_e32 v7, v7, v50
	v_mul_f32_e32 v8, v8, v51
	v_mul_f32_e32 v9, v36, v9
	v_mul_f32_e32 v10, v37, v10
	v_rcp_f32_e32 v11, v11
	v_rcp_f32_e32 v12, v12
	v_mul_f32_e32 v9, v9, v40
	v_mul_f32_e32 v10, v10, v41
	v_med3_f32 v2, v7, s7, v228
	v_med3_f32 v7, v8, s7, v228
	v_cvt_pk_fp8_f32 v6, v2, v7 op_sel:[0,0,1]
	v_med3_f32 v2, v9, s7, v228
	v_med3_f32 v8, v10, s7, v228
	v_mov_b32_e32 v7, v3
	v_cvt_pk_fp8_f32 v7, v2, v8
	v_mul_f32_e32 v11, v38, v11
	v_mul_f32_e32 v12, v39, v12
	v_mul_f32_e32 v11, v11, v42
	v_mul_f32_e32 v12, v12, v43
	v_med3_f32 v2, v11, s7, v228
	v_med3_f32 v8, v12, s7, v228
	v_cvt_pk_fp8_f32 v7, v2, v8 op_sel:[0,0,1]
	v_add_co_u32_e32 v4, vcc, 0x58000, v4
	v_mov_b32_e32 v176, v204
	s_nop 0
	v_addc_co_u32_e32 v5, vcc, 0, v5, vcc
	s_and_b64 vcc, exec, s[38:39]
	v_mov_b32_e32 v178, v205
	v_mov_b32_e32 v180, v203
	v_mov_b32_e32 v184, v202
	s_mov_b32 s3, s44
	s_mov_b32 s48, s42
	s_mov_b64 s[50:51], s[46:47]
	global_store_dwordx2 v[4:5], v[6:7], off
	s_lshl_b32 s72, s32, 8
	s_add_i32 s72, s72, s2
	s_add_i32 s32, s32, 2
	s_cmpk_ge_i32 s72, 7136
	s_cbranch_scc1 .Lcvd_p2_end
	v_readlane_b32 s78, v255, 42
	v_readlane_b32 s79, v255, 43
	s_addk_i32 s72, 1056
	s_lshr_b32 s80, s72, 9
	s_lshl_b32 s80, s80, 21
	s_and_b32 s81, s72, 15
	s_lshl_b32 s81, s81, 17
	s_add_i32 s80, s80, s81
	s_bfe_u32 s81, s72, 0x50004
	s_lshl_b32 s81, s81, 6
	s_add_i32 s80, s80, s81
	v_and_b32_e32 v230, 63, v0
	v_lshlrev_b32_e32 v230, 11, v230
	v_add_u32_e32 v231, s80, v230
	s_waitcnt vmcnt(8)
	v_mul_f32_e32 v210, 0x42800000, v210
	v_mul_f32_e32 v211, 0x42800000, v211
	v_mul_f32_e32 v212, 0x42800000, v212
	v_mul_f32_e32 v213, 0x42800000, v213
	v_mul_f32_e32 v214, 0x42800000, v214
	v_mul_f32_e32 v215, 0x42800000, v215
	v_mul_f32_e32 v216, 0x42800000, v216
	v_mul_f32_e32 v217, 0x42800000, v217
	v_med3_f32 v210, v210, s7, v228
	v_med3_f32 v211, v211, s7, v228
	v_med3_f32 v212, v212, s7, v228
	v_med3_f32 v213, v213, s7, v228
	v_med3_f32 v214, v214, s7, v228
	v_med3_f32 v215, v215, s7, v228
	v_med3_f32 v216, v216, s7, v228
	v_med3_f32 v217, v217, s7, v228
	v_cvt_pk_fp8_f32 v232, v210, v211
	v_cvt_pk_fp8_f32 v233, v214, v215
	v_cvt_pk_fp8_f32 v232, v212, v213 op_sel:[0,0,1]
	v_cvt_pk_fp8_f32 v233, v216, v217 op_sel:[0,0,1]
	s_nop 1
	global_store_dwordx2 v231, v[232:233], s[78:79] nt
	s_cmpk_ge_i32 s72, 7936
	s_cbranch_scc1 .Lcvd_p2_end
	s_addk_i32 s72, 0x100
	s_lshr_b32 s80, s72, 9
	s_lshl_b32 s80, s80, 21
	s_and_b32 s81, s72, 15
	s_lshl_b32 s81, s81, 17
	s_add_i32 s80, s80, s81
	s_bfe_u32 s81, s72, 0x50004
	s_lshl_b32 s81, s81, 6
	s_add_i32 s80, s80, s81
	v_add_u32_e32 v236, s80, v230
	v_mul_f32_e32 v218, 0x42800000, v218
	v_mul_f32_e32 v219, 0x42800000, v219
	v_mul_f32_e32 v220, 0x42800000, v220
	v_mul_f32_e32 v221, 0x42800000, v221
	v_mul_f32_e32 v222, 0x42800000, v222
	v_mul_f32_e32 v223, 0x42800000, v223
	v_mul_f32_e32 v224, 0x42800000, v224
	v_mul_f32_e32 v225, 0x42800000, v225
	v_med3_f32 v218, v218, s7, v228
	v_med3_f32 v219, v219, s7, v228
	v_med3_f32 v220, v220, s7, v228
	v_med3_f32 v221, v221, s7, v228
	v_med3_f32 v222, v222, s7, v228
	v_med3_f32 v223, v223, s7, v228
	v_med3_f32 v224, v224, s7, v228
	v_med3_f32 v225, v225, s7, v228
	v_cvt_pk_fp8_f32 v234, v218, v219
	v_cvt_pk_fp8_f32 v235, v222, v223
	v_cvt_pk_fp8_f32 v234, v220, v221 op_sel:[0,0,1]
	v_cvt_pk_fp8_f32 v235, v224, v225 op_sel:[0,0,1]
	s_nop 1
	global_store_dwordx2 v236, v[234:235], s[78:79] nt
